# non-temporal hint on the final f32 output stores (never re-read in the launch)
# speedup vs baseline: 1.0005x; 1.0005x over previous
; #define GAS __attribute__((address_space(1)))
; #define SB() __builtin_amdgcn_sched_barrier(0)
; __device__ __forceinline__ float bflo(unsigned w) { return __uint_as_float(w << 16); }
; __device__ __forceinline__ float bfhi(unsigned w) { return __uint_as_float(w & 0xffff0000u); }
; template <int COMBINE, int DO_NORM>
; __device__ __forceinline__ void norm1_phase(Frame& F, int l, const float* xsrc) {
;     ...
;     for (int row = F.gw; row < T; row += F.NGW) {
;         const float* xr = xsrc + (size_t)row * D; unsigned lo16 = (unsigned)F.lane * 16u; asm volatile("" : "+v"(lo16)); const unsigned lo8 = lo16 >> 1;
;         f32x4 v[8];
;         if (COMBINE) {
;             const int t0 = WSP(int, WS_TOK)[row * 2], t1 = WSP(int, WS_TOK)[row * 2 + 1];
;             const int b0 = (int)tbase[t0 >> 16], b1 = (int)tbase[t1 >> 16];
;             const bf16_t* y0 = WSP(bf16_t, WS_Y) + (size_t)(b0 + (t0 & 0xffff)) * D;
;             const bf16_t* y1 = WSP(bf16_t, WS_Y) + (size_t)(b1 + (t1 & 0xffff)) * D;
;             u32x2 ya[8], yb[8], xa[8]; const bf16_t* xb = WSP(bf16_t, WS_XB) + (size_t)row * D;
; #pragma unroll
;             for (int j = 0; j < 8; ++j) { xa[j] = ldg8(xb, lo8 + 512u * j); ya[j] = ldg8(y0, lo8 + 512u * j); yb[j] = ldg8(y1, lo8 + 512u * j); }
;             SB();
;             GAS f32x4* xo = (GAS f32x4*)(F.out + (size_t)row * D) + F.lane; GAS u32x2* xbo = (GAS u32x2*)(WSP(bf16_t, WS_XB) + (size_t)row * D) + F.lane;
; #pragma unroll
;             for (int j = 0; j < 8; ++j) { const u32x2 a = ya[j], b = yb[j], x = xa[j];
;                 v[j].x = bflo(x.x) + (bflo(a.x) + bflo(b.x)); v[j].y = bfhi(x.x) + (bfhi(a.x) + bfhi(b.x)); v[j].z = bflo(x.y) + (bflo(a.y) + bflo(b.y)); v[j].w = bfhi(x.y) + (bfhi(a.y) + bfhi(b.y));
.LBB0_1699:
	s_ashr_i32 s3, s2, 31
	s_lshl_b64 s[10:11], s[2:3], 2
	s_add_u32 s10, s8, s10
	v_mov_b32_e32 v4, v18
	s_addc_u32 s11, s9, s11
	global_load_dwordx2 v[2:3], v19, s[10:11]
	v_lshrrev_b32_e32 v11, 1, v4
	s_waitcnt vmcnt(0)
	v_readfirstlane_b32 s3, v2
	s_ashr_i32 s10, s3, 16
	s_ashr_i32 s11, s10, 31
	s_lshl_b64 s[10:11], s[10:11], 2
	v_readfirstlane_b32 s12, v3
	s_add_u32 s10, s6, s10
	s_addc_u32 s11, s7, s11
	s_ashr_i32 s12, s12, 16
	s_ashr_i32 s13, s12, 31
	global_load_dword v8, v19, s[10:11]
	s_lshl_b64 s[10:11], s[12:13], 2
	s_add_u32 s10, s6, s10
	s_addc_u32 s11, s7, s11
	global_load_dword v10, v19, s[10:11]
	global_load_dwordx2 v[6:7], v11, s[4:5] offset:-3584
	global_load_dwordx2 v[20:21], v11, s[4:5] offset:-3072
	global_load_dwordx2 v[22:23], v11, s[4:5] offset:-2560
	global_load_dwordx2 v[24:25], v11, s[4:5] offset:-2048
	global_load_dwordx2 v[26:27], v11, s[4:5] offset:-1536
	global_load_dwordx2 v[28:29], v11, s[4:5] offset:-1024
	global_load_dwordx2 v[30:31], v11, s[4:5] offset:-512
	global_load_dwordx2 v[4:5], v11, s[4:5]
	s_waitcnt vmcnt(9)
	v_add_u32_sdwa v8, v8, v2 dst_sel:DWORD dst_unused:UNUSED_PAD src0_sel:DWORD src1_sel:WORD_0
	v_ashrrev_i32_e32 v9, 31, v8
	v_lshlrev_b64 v[8:9], 12, v[8:9]
	v_lshl_add_u64 v[8:9], s[0:1], 0, v[8:9]
	s_waitcnt vmcnt(8)
	v_add_u32_sdwa v2, v10, v3 dst_sel:DWORD dst_unused:UNUSED_PAD src0_sel:DWORD src1_sel:WORD_0
	v_ashrrev_i32_e32 v3, 31, v2
	v_lshlrev_b64 v[2:3], 12, v[2:3]
	v_readfirstlane_b32 s10, v8
	v_readfirstlane_b32 s11, v9
	v_lshl_add_u64 v[2:3], s[0:1], 0, v[2:3]
	s_nop 3
	global_load_dwordx2 v[16:17], v11, s[10:11]
	global_load_dwordx2 v[32:33], v11, s[10:11] offset:512
	global_load_dwordx2 v[34:35], v11, s[10:11] offset:1024
	global_load_dwordx2 v[36:37], v11, s[10:11] offset:1536
	global_load_dwordx2 v[38:39], v11, s[10:11] offset:2048
	global_load_dwordx2 v[40:41], v11, s[10:11] offset:2560
	global_load_dwordx2 v[42:43], v11, s[10:11] offset:3072
	global_load_dwordx2 v[8:9], v11, s[10:11] offset:3584
	v_readfirstlane_b32 s10, v2
	v_readfirstlane_b32 s11, v3
	s_nop 4
	global_load_dwordx2 v[44:45], v11, s[10:11]
	global_load_dwordx2 v[46:47], v11, s[10:11] offset:512
	global_load_dwordx2 v[48:49], v11, s[10:11] offset:1024
	global_load_dwordx2 v[50:51], v11, s[10:11] offset:1536
	global_load_dwordx2 v[52:53], v11, s[10:11] offset:2048
	global_load_dwordx2 v[54:55], v11, s[10:11] offset:2560
	global_load_dwordx2 v[56:57], v11, s[10:11] offset:3072
	global_load_dwordx2 v[14:15], v11, s[10:11] offset:3584
	s_waitcnt vmcnt(15)
	v_lshlrev_b32_e32 v10, 16, v16
	v_and_b32_e32 v11, 0xffff0000, v16
	s_waitcnt vmcnt(7)
	v_lshlrev_b32_e32 v12, 16, v44
	v_and_b32_e32 v13, 0xffff0000, v44
	v_lshlrev_b32_e32 v58, 16, v17
	v_and_b32_e32 v59, 0xffff0000, v17
	v_lshlrev_b32_e32 v44, 16, v45
	v_and_b32_e32 v45, 0xffff0000, v45
	s_add_i32 s76, s76, s84
	s_add_i32 s2, s2, s85
	v_lshlrev_b32_e32 v2, 16, v6
	v_and_b32_e32 v3, 0xffff0000, v6
	v_lshlrev_b32_e32 v6, 16, v7
	v_and_b32_e32 v7, 0xffff0000, v7
	v_lshlrev_b32_e32 v60, 16, v32
	v_and_b32_e32 v61, 0xffff0000, v32
	s_waitcnt vmcnt(6)
	v_lshlrev_b32_e32 v62, 16, v46
	v_and_b32_e32 v63, 0xffff0000, v46
	v_lshlrev_b32_e32 v32, 16, v33
	v_and_b32_e32 v33, 0xffff0000, v33
	v_lshlrev_b32_e32 v46, 16, v47
	v_and_b32_e32 v47, 0xffff0000, v47
	v_lshlrev_b32_e32 v66, 16, v34
	v_and_b32_e32 v67, 0xffff0000, v34
	s_waitcnt vmcnt(5)
	v_lshlrev_b32_e32 v68, 16, v48
	v_and_b32_e32 v69, 0xffff0000, v48
	v_lshlrev_b32_e32 v34, 16, v35
	v_and_b32_e32 v35, 0xffff0000, v35
	v_lshlrev_b32_e32 v48, 16, v49
	v_and_b32_e32 v49, 0xffff0000, v49
	v_lshlrev_b32_e32 v72, 16, v36
	v_and_b32_e32 v73, 0xffff0000, v36
	s_waitcnt vmcnt(4)
	v_lshlrev_b32_e32 v74, 16, v50
	v_and_b32_e32 v75, 0xffff0000, v50
	v_lshlrev_b32_e32 v36, 16, v37
	v_and_b32_e32 v37, 0xffff0000, v37
	v_lshlrev_b32_e32 v50, 16, v51
	v_and_b32_e32 v51, 0xffff0000, v51
	v_lshlrev_b32_e32 v78, 16, v38
	v_and_b32_e32 v79, 0xffff0000, v38
	s_waitcnt vmcnt(3)
; __device__ __forceinline__ unsigned cvt_pk_bf16(float lo, float hi) { unsigned r; asm volatile("v_cvt_pk_bf16_f32 %0, %1, %2" : "=v"(r) : "v"(lo), "v"(hi)); return r; }
; __device__ __forceinline__ float bflo(unsigned w) { return __uint_as_float(w << 16); }
; __device__ __forceinline__ float bfhi(unsigned w) { return __uint_as_float(w & 0xffff0000u); }
; template <int COMBINE, int DO_NORM>
; __device__ __forceinline__ void norm1_phase(Frame& F, int l, const float* xsrc) {
;     ...
;             for (int j = 0; j < 8; ++j) { const u32x2 a = ya[j], b = yb[j], x = xa[j];
;                 v[j].x = bflo(x.x) + (bflo(a.x) + bflo(b.x)); v[j].y = bfhi(x.x) + (bfhi(a.x) + bfhi(b.x)); v[j].z = bflo(x.y) + (bflo(a.y) + bflo(b.y)); v[j].w = bfhi(x.y) + (bfhi(a.y) + bfhi(b.y));
;                 if (DO_NORM) { u32x2 w; w.x = cvt_pk_bf16(v[j].x, v[j].y); w.y = cvt_pk_bf16(v[j].z, v[j].w); xbo[64 * j] = w; }
;                 else xo[64 * j] = v[j]; }
	v_lshlrev_b32_e32 v80, 16, v52
	v_and_b32_e32 v81, 0xffff0000, v52
	v_lshlrev_b32_e32 v38, 16, v39
	v_and_b32_e32 v39, 0xffff0000, v39
	v_lshlrev_b32_e32 v52, 16, v53
	v_and_b32_e32 v53, 0xffff0000, v53
	v_lshlrev_b32_e32 v84, 16, v40
	v_and_b32_e32 v85, 0xffff0000, v40
	s_waitcnt vmcnt(2)
	v_lshlrev_b32_e32 v86, 16, v54
	v_and_b32_e32 v87, 0xffff0000, v54
	v_lshlrev_b32_e32 v40, 16, v41
	v_and_b32_e32 v41, 0xffff0000, v41
	v_lshlrev_b32_e32 v54, 16, v55
	v_and_b32_e32 v55, 0xffff0000, v55
	v_lshlrev_b32_e32 v90, 16, v42
	v_and_b32_e32 v91, 0xffff0000, v42
	s_waitcnt vmcnt(1)
	v_lshlrev_b32_e32 v92, 16, v56
	v_and_b32_e32 v93, 0xffff0000, v56
	v_lshlrev_b32_e32 v42, 16, v43
	v_and_b32_e32 v43, 0xffff0000, v43
	v_lshlrev_b32_e32 v56, 16, v57
	v_and_b32_e32 v57, 0xffff0000, v57
	v_lshlrev_b32_e32 v94, 16, v4
	v_and_b32_e32 v95, 0xffff0000, v4
	v_lshlrev_b32_e32 v96, 16, v8
	v_and_b32_e32 v97, 0xffff0000, v8
	s_waitcnt vmcnt(0)
	v_lshlrev_b32_e32 v98, 16, v14
	v_and_b32_e32 v99, 0xffff0000, v14
	v_lshlrev_b32_e32 v100, 16, v5
	v_and_b32_e32 v101, 0xffff0000, v5
	v_lshlrev_b32_e32 v4, 16, v9
	v_and_b32_e32 v5, 0xffff0000, v9
	v_lshlrev_b32_e32 v8, 16, v15
	v_and_b32_e32 v9, 0xffff0000, v15
	v_pk_add_f32 v[10:11], v[10:11], v[12:13]
	v_pk_add_f32 v[12:13], v[58:59], v[44:45]
	s_add_u32 s4, s4, s16
	v_lshlrev_b32_e32 v16, 16, v20
	v_and_b32_e32 v17, 0xffff0000, v20
	v_lshlrev_b32_e32 v20, 16, v21
	v_and_b32_e32 v21, 0xffff0000, v21
	v_lshlrev_b32_e32 v64, 16, v22
	v_and_b32_e32 v65, 0xffff0000, v22
	v_lshlrev_b32_e32 v22, 16, v23
	v_and_b32_e32 v23, 0xffff0000, v23
	v_lshlrev_b32_e32 v70, 16, v24
	v_and_b32_e32 v71, 0xffff0000, v24
	v_lshlrev_b32_e32 v24, 16, v25
	v_and_b32_e32 v25, 0xffff0000, v25
	v_lshlrev_b32_e32 v76, 16, v26
	v_and_b32_e32 v77, 0xffff0000, v26
	v_lshlrev_b32_e32 v26, 16, v27
	v_and_b32_e32 v27, 0xffff0000, v27
	v_lshlrev_b32_e32 v82, 16, v28
	v_and_b32_e32 v83, 0xffff0000, v28
	v_lshlrev_b32_e32 v28, 16, v29
	v_and_b32_e32 v29, 0xffff0000, v29
	v_lshlrev_b32_e32 v88, 16, v30
	v_and_b32_e32 v89, 0xffff0000, v30
	v_lshlrev_b32_e32 v30, 16, v31
	v_and_b32_e32 v31, 0xffff0000, v31
	v_pk_add_f32 v[14:15], v[60:61], v[62:63]
	v_pk_add_f32 v[32:33], v[32:33], v[46:47]
	v_pk_add_f32 v[44:45], v[66:67], v[68:69]
	v_pk_add_f32 v[34:35], v[34:35], v[48:49]
	v_pk_add_f32 v[46:47], v[72:73], v[74:75]
	v_pk_add_f32 v[36:37], v[36:37], v[50:51]
	v_pk_add_f32 v[48:49], v[78:79], v[80:81]
	v_pk_add_f32 v[38:39], v[38:39], v[52:53]
	v_pk_add_f32 v[50:51], v[84:85], v[86:87]
	v_pk_add_f32 v[40:41], v[40:41], v[54:55]
	v_pk_add_f32 v[52:53], v[90:91], v[92:93]
	v_pk_add_f32 v[42:43], v[42:43], v[56:57]
	v_pk_add_f32 v[54:55], v[96:97], v[98:99]
	v_pk_add_f32 v[56:57], v[4:5], v[8:9]
	v_pk_add_f32 v[2:3], v[10:11], v[2:3]
	v_pk_add_f32 v[4:5], v[12:13], v[6:7]
	s_addc_u32 s5, s5, s17
	v_pk_add_f32 v[6:7], v[14:15], v[16:17]
	v_pk_add_f32 v[8:9], v[32:33], v[20:21]
	v_pk_add_f32 v[10:11], v[44:45], v[64:65]
	v_pk_add_f32 v[12:13], v[34:35], v[22:23]
	v_pk_add_f32 v[14:15], v[46:47], v[70:71]
	v_pk_add_f32 v[16:17], v[36:37], v[24:25]
	v_pk_add_f32 v[20:21], v[48:49], v[76:77]
	v_pk_add_f32 v[22:23], v[38:39], v[26:27]
	v_pk_add_f32 v[24:25], v[50:51], v[82:83]
	v_pk_add_f32 v[26:27], v[40:41], v[28:29]
	v_pk_add_f32 v[28:29], v[52:53], v[88:89]
	v_pk_add_f32 v[30:31], v[42:43], v[30:31]
	v_pk_add_f32 v[32:33], v[54:55], v[94:95]
	v_pk_add_f32 v[34:35], v[56:57], v[100:101]
	global_store_dwordx4 v[0:1], v[2:5], off offset:-4096 nt
	global_store_dwordx4 v[0:1], v[6:9], off offset:-3072 nt
	global_store_dwordx4 v[0:1], v[10:13], off offset:-2048 nt
	global_store_dwordx4 v[0:1], v[14:17], off offset:-1024 nt
	global_store_dwordx4 v[0:1], v[20:23], off nt
	global_store_dwordx4 v[0:1], v[24:27], off offset:1024 nt
	global_store_dwordx4 v[0:1], v[28:31], off offset:2048 nt
	global_store_dwordx4 v[0:1], v[32:35], off offset:3072 nt
	s_cmpk_lt_i32 s76, 0x2000
	v_lshl_add_u64 v[0:1], v[0:1], 0, s[14:15]
	s_cbranch_scc1 .LBB0_1699
